# MLA step: the s_nop 0 behind M0 writes covered by reordered independent instructions and the s_nop 0 in front of the row max removed (7 instructions less per two steps in an issue-bound loop)
# baseline (speedup 1.0000x reference)
.LBB0_1149:
	s_setprio 1
	s_waitcnt lgkmcnt(0)
	v_mfma_f32_32x32x16_bf16 v[100:115], v[202:205], v[136:139], v[36:51]
	s_add_i32 s19, s27, -1
	s_and_b32 s18, s19, 3
	s_mul_i32 s20, s18, 0x3000
	s_and_b32 s17, s14, 0x6000
	s_add_i32 s16, s27, 2
	s_min_i32 s8, s16, s2
	s_lshl_b64 s[10:11], s[8:9], 17
	v_lshl_add_u64 v[154:155], v[176:177], 0, s[10:11]
	s_and_b32 s10, s16, 3
	s_mulk_i32 s10, 0x3000
	s_add_i32 s10, s26, s10
	s_mov_b32 m0, s10
	ds_read_b128 v[202:205], v156 offset:4096
	global_load_lds_dwordx4 v[154:155], off
	v_mfma_f32_32x32x16_bf16 v[84:99], v[190:193], v[136:139], v[36:51]
	s_and_b64 vcc, exec, s[38:39]
	s_cbranch_vccnz .Lmla_rope1
	s_add_i32 m0, s10, 0x2000
	s_lshl_b64 s[12:13], s[8:9], 18
	v_lshl_add_u64 v[154:155], v[180:181], 0, s[12:13]
	global_load_lds_dwordx4 v[154:155], off
.Lmla_rope1:
	ds_read_b128 v[190:193], v156 offset:4608
	v_mfma_f32_32x32x16_bf16 v[100:115], v[194:197], v[132:135], v[100:115]
	s_add_i32 s8, s27, 1
	s_min_i32 s8, s8, s2
	s_lshl_b32 s8, s8, 17
	v_lshl_add_u64 v[154:155], v[178:179], 0, s[8:9]
	s_add_i32 s8, s14, 0xffffe000
	s_and_b32 s15, s8, 0x6000
	s_add_i32 s8, s26, s15
	s_add_i32 m0, s8, 0xc000
	v_lshl_add_u64 v[154:155], v[154:155], 0, s[24:25]
	global_load_lds_dwordx4 v[154:155], off
	ds_read_b128 v[194:197], v156 offset:6144
	v_mfma_f32_32x32x16_bf16 v[84:99], v[198:201], v[132:135], v[84:99]
	ds_read_b128 v[198:201], v156 offset:6656
	v_exp_f32_e32 v60, v60
	v_exp_f32_e32 v61, v61
	v_exp_f32_e32 v62, v62
	v_exp_f32_e32 v63, v63
	s_waitcnt lgkmcnt(0)
	v_mfma_f32_32x32x16_bf16 v[100:115], v[202:205], v[128:131], v[100:115]
	ds_read_b128 v[202:205], v156 offset:8192
	v_exp_f32_e32 v64, v64
	v_exp_f32_e32 v65, v65
	v_exp_f32_e32 v66, v66
	v_exp_f32_e32 v67, v67
	v_mfma_f32_32x32x16_bf16 v[84:99], v[190:193], v[128:131], v[84:99]
	ds_read_b128 v[190:193], v156 offset:8704
	v_add_f32_e32 v162, v68, v69
	ds_read_b64_tr_b16 v[172:173], v157 offset:49152
	ds_read_b64_tr_b16 v[174:175], v157 offset:49664
	v_add_f32_e32 v161, v70, v162
	v_add_f32_e32 v161, v71, v161
	v_add_f32_e32 v161, v72, v161
	v_add_f32_e32 v144, v73, v161
	v_cvt_pk_bf16_f32 v140, v68, v69
	v_mfma_f32_32x32x16_bf16 v[100:115], v[194:197], v[124:127], v[100:115]
	ds_read_b128 v[194:197], v156 offset:10240
	v_cvt_pk_bf16_f32 v141, v70, v71
	ds_read_b64_tr_b16 v[68:69], v157 offset:53248
	ds_read_b64_tr_b16 v[70:71], v157 offset:53760
	v_add_f32_e32 v142, v74, v144
	v_add_f32_e32 v142, v75, v142
	v_add_f32_e32 v142, v76, v142
	v_add_f32_e32 v144, v77, v142
	v_cvt_pk_bf16_f32 v142, v72, v73
	v_mfma_f32_32x32x16_bf16 v[84:99], v[198:201], v[124:127], v[84:99]
	ds_read_b128 v[198:201], v156 offset:10752
	v_cvt_pk_bf16_f32 v143, v74, v75
	ds_read_b64_tr_b16 v[72:73], v157 offset:50176
	ds_read_b64_tr_b16 v[74:75], v157 offset:50688
	v_add_f32_e32 v144, v78, v144
	v_add_f32_e32 v144, v79, v144
	v_add_f32_e32 v144, v80, v144
	v_add_f32_e32 v148, v81, v144
	v_cvt_pk_bf16_f32 v144, v76, v77
	s_waitcnt lgkmcnt(0)
	v_mfma_f32_32x32x16_bf16 v[100:115], v[202:205], v[120:123], v[100:115]
	v_cvt_pk_bf16_f32 v145, v78, v79
	ds_read_b64_tr_b16 v[76:77], v157 offset:54272
	ds_read_b64_tr_b16 v[78:79], v157 offset:54784
	v_add_f32_e32 v146, v82, v148
	v_add_f32_e32 v146, v83, v146
	v_add_f32_e32 v146, v52, v146
	v_add_f32_e32 v148, v53, v146
	v_cvt_pk_bf16_f32 v146, v80, v81
	v_cvt_pk_bf16_f32 v147, v82, v83
	ds_read_b64_tr_b16 v[80:81], v157 offset:51200
	v_mfma_f32_32x32x16_bf16 v[84:99], v[190:193], v[120:123], v[84:99]
	ds_read_b64_tr_b16 v[82:83], v157 offset:51712
	v_add_f32_e32 v148, v54, v148
	v_add_f32_e32 v148, v55, v148
	v_add_f32_e32 v148, v56, v148
	v_add_f32_e32 v152, v57, v148
	v_cvt_pk_bf16_f32 v148, v52, v53
	v_cvt_pk_bf16_f32 v149, v54, v55
	ds_read_b64_tr_b16 v[52:53], v157 offset:55296
	ds_read_b64_tr_b16 v[54:55], v157 offset:55808
	v_add_f32_e32 v150, v58, v152
	v_mfma_f32_32x32x16_bf16 v[100:115], v[194:197], v[116:119], v[100:115]
	v_add_f32_e32 v150, v59, v150
	v_add_f32_e32 v150, v60, v150
	v_add_f32_e32 v152, v61, v150
	v_cvt_pk_bf16_f32 v150, v56, v57
	v_cvt_pk_bf16_f32 v151, v58, v59
	ds_read_b64_tr_b16 v[56:57], v157 offset:52224
	ds_read_b64_tr_b16 v[58:59], v157 offset:52736
	v_add_f32_e32 v152, v62, v152
	v_add_f32_e32 v152, v63, v152
	v_add_f32_e32 v152, v64, v152
	v_mfma_f32_32x32x16_bf16 v[84:99], v[198:201], v[116:119], v[84:99]
	v_add_f32_e32 v160, v65, v152
	v_cvt_pk_bf16_f32 v152, v60, v61
	v_cvt_pk_bf16_f32 v153, v62, v63
	ds_read_b64_tr_b16 v[60:61], v157 offset:56320
	ds_read_b64_tr_b16 v[62:63], v157 offset:56832
	v_add_f32_e32 v154, v66, v160
	v_add_f32_e32 v156, v67, v154
	v_cvt_pk_bf16_f32 v154, v64, v65
	v_cvt_pk_bf16_f32 v155, v66, v67
	s_setprio 0
	s_cmp_lt_i32 s19, s52
	s_cbranch_scc0 .LBB0_1167
.LBB0_1152:
	v_max_f32_e32 v64, v101, v100
	v_max3_f32 v65, v102, v103, v85
	v_max3_f32 v64, v64, v84, v86
	v_max3_f32 v64, v64, v87, v104
	v_max3_f32 v65, v65, v106, v107
	v_max3_f32 v64, v64, v105, v88
	v_max3_f32 v65, v65, v90, v91
	v_max3_f32 v64, v64, v89, v108
	v_max3_f32 v65, v65, v110, v111
	v_max3_f32 v64, v64, v109, v92
	v_max3_f32 v65, v65, v94, v95
	v_max3_f32 v64, v64, v93, v112
	v_max3_f32 v65, v65, v114, v115
	v_max3_f32 v64, v64, v113, v96
	v_max3_f32 v65, v65, v98, v99
	v_max3_f32 v64, v64, v97, v65
	v_mov_b32_e32 v65, v64
	s_nop 1
	v_permlane32_swap_b32_e32 v64, v65
	v_max_f32_e32 v64, v64, v65
	v_cmp_lt_f32_e32 vcc, s81, v64
	s_cmp_lg_u64 vcc, 0
	v_add_f32_e32 v189, v189, v156
	s_cselect_b64 s[10:11], -1, 0
	s_cbranch_vccnz .LBB0_1168

.LBB0_1159:
	s_setprio 1
	s_waitcnt lgkmcnt(0)
	v_mfma_f32_32x32x16_bf16 v[68:83], v[202:205], v[136:139], v[36:51]
	s_add_i32 s8, s27, 3
	s_min_i32 s8, s8, s2
	s_lshl_b64 s[10:11], s[8:9], 17
	v_lshl_add_u64 v[170:171], v[176:177], 0, s[10:11]
	s_add_i32 s10, s26, s20
	s_mov_b32 m0, s10
	ds_read_b128 v[202:205], v140 offset:4096
	global_load_lds_dwordx4 v[170:171], off
	v_mfma_f32_32x32x16_bf16 v[52:67], v[190:193], v[136:139], v[36:51]
	s_and_b64 vcc, exec, s[38:39]
	s_cbranch_vccnz .Lmla_rope2
	s_add_i32 m0, s10, 0x2000
	s_lshl_b64 s[12:13], s[8:9], 18
	v_lshl_add_u64 v[170:171], v[180:181], 0, s[12:13]
	global_load_lds_dwordx4 v[170:171], off

; __device__ __forceinline__ float swapmax(float m) { auto rr = __builtin_amdgcn_permlane32_swap(__float_as_uint(m), __float_as_uint(m), false, false); return fmaxf(__uint_as_float(rr[0]), __uint_as_float(rr[1])); }
; #define ATT_MX3(a, b, c) __builtin_fmaxf(__builtin_fmaxf((a), (b)), (c))
; __device__ __forceinline__ float rowmax(const f32x16& p0, const f32x16& p1) {
;     float a = ATT_MX3(p0[0], p0[1], p1[0]), b = ATT_MX3(p0[2], p0[3], p1[1]); a = ATT_MX3(a, p1[2], p1[3]);
; #pragma unroll
;     for (int r = 4; r < 16; r += 4) { a = ATT_MX3(a, p0[r], p0[r + 1]); b = ATT_MX3(b, p0[r + 2], p0[r + 3]); a = ATT_MX3(a, p1[r], p1[r + 1]); b = ATT_MX3(b, p1[r + 2], p1[r + 3]); }
;     return swapmax(__builtin_fmaxf(a, b));
; }
.LBB0_1162:
	v_max_f32_e32 v96, v69, v68
	v_max3_f32 v97, v70, v71, v53
	v_max3_f32 v96, v96, v52, v54
	v_max3_f32 v96, v96, v55, v72
	v_max3_f32 v97, v97, v74, v75
	v_max3_f32 v96, v96, v73, v56
	v_max3_f32 v97, v97, v58, v59
	v_max3_f32 v96, v96, v57, v76
	v_max3_f32 v97, v97, v78, v79
	v_max3_f32 v96, v96, v77, v60
	v_max3_f32 v97, v97, v62, v63
	v_max3_f32 v96, v96, v61, v80
	v_max3_f32 v97, v97, v82, v83
	v_max3_f32 v96, v96, v81, v64
	v_max3_f32 v97, v97, v66, v67
	v_max3_f32 v96, v96, v65, v97
	v_mov_b32_e32 v97, v96
	s_nop 1
	v_permlane32_swap_b32_e32 v96, v97
	v_max_f32_e32 v96, v96, v97
	v_cmp_lt_f32_e32 vcc, s81, v96
	s_cmp_lg_u64 vcc, 0
	v_add_f32_e32 v189, v189, v140
	s_cselect_b64 s[10:11], -1, 0
	s_cbranch_vccnz .LBB0_1172
